# attention tile loops: second batch of V^T fragment reads issued before the first P V MFMA group (free registers), latency covered by MFMAs
# speedup vs baseline: 1.0027x; 1.0027x over previous
.LBB0_1598:
	ds_read_b128 v[36:39], v211 offset:12288
	ds_read_b128 v[52:55], v211 offset:12320
	ds_read_b128 v[56:59], v211 offset:18432
	ds_read_b128 v[60:63], v211 offset:18464
	v_exp_f32_e32 v84, v116
	v_exp_f32_e32 v98, v132
	s_waitcnt lgkmcnt(0)
	v_mfma_f32_32x32x16_bf16 v[36:51], v[36:39], v[168:171], 0
	v_exp_f32_e32 v85, v117
	v_exp_f32_e32 v116, v133
	v_exp_f32_e32 v117, v118
	v_exp_f32_e32 v118, v134
	v_exp_f32_e32 v125, v125
	v_exp_f32_e32 v132, v141
	v_exp_f32_e32 v129, v129
	v_mfma_f32_32x32x16_bf16 v[68:83], v[56:59], v[168:171], 0
	v_cvt_pk_bf16_f32 v84, v84, v85
	v_mfma_f32_32x32x16_bf16 v[36:51], v[52:55], v[148:151], v[36:51]
	ds_read_b128 v[52:55], v211 offset:12352
	ds_read_b128 v[56:59], v211 offset:12384
	v_mfma_f32_32x32x16_bf16 v[68:83], v[60:63], v[148:151], v[68:83]
	v_exp_f32_e32 v61, v126
	v_exp_f32_e32 v126, v142
	v_exp_f32_e32 v62, v127
	v_exp_f32_e32 v127, v143
	v_exp_f32_e32 v63, v128
	v_exp_f32_e32 v128, v144
	v_cvt_pk_bf16_f32 v61, v61, v62
	s_waitcnt lgkmcnt(0)
	v_mfma_f32_32x32x16_bf16 v[36:51], v[52:55], v[152:155], v[36:51]
	ds_read_b128 v[52:55], v211 offset:18496
	ds_read_b128 v[86:89], v211 offset:18528
	ds_read_b128 v[90:93], v226 offset:12288
	ds_read_b128 v[94:97], v226 offset:18432
	v_cvt_pk_bf16_f32 v62, v63, v129
	s_waitcnt lgkmcnt(0)
	v_mfma_f32_32x32x16_bf16 v[68:83], v[52:55], v[152:155], v[68:83]
	v_exp_f32_e32 v54, v145
	v_exp_f32_e32 v52, v130
	v_exp_f32_e32 v55, v146
	v_exp_f32_e32 v53, v131
	v_exp_f32_e32 v130, v147
	v_cvt_pk_bf16_f32 v54, v128, v54
	v_cvt_pk_bf16_f32 v63, v52, v53
	v_mfma_f32_32x32x16_bf16 v[36:51], v[56:59], v[156:159], v[36:51]
	ds_read_b128 v[56:59], v227 offset:12288
	ds_read_b128 v[236:239], v227 offset:18432
	v_cvt_pk_bf16_f32 v53, v126, v127
	v_cvt_pk_bf16_f32 v55, v55, v130
	v_mfma_f32_32x32x16_bf16 v[68:83], v[86:89], v[156:159], v[68:83]
	v_mfma_f32_32x32x16_bf16 v[36:51], v[90:93], v[160:163], v[36:51]
	v_exp_f32_e32 v90, v119
	v_exp_f32_e32 v91, v135
	v_exp_f32_e32 v92, v120
	v_exp_f32_e32 v93, v136
	v_exp_f32_e32 v119, v121
	v_exp_f32_e32 v120, v137
	v_exp_f32_e32 v121, v122
	v_mfma_f32_32x32x16_bf16 v[68:83], v[94:97], v[160:163], v[68:83]
	v_exp_f32_e32 v122, v139
	v_cvt_pk_bf16_f32 v85, v117, v90
	v_cvt_pk_bf16_f32 v86, v92, v119
	s_waitcnt lgkmcnt(0)
	v_mfma_f32_32x32x16_bf16 v[36:51], v[56:59], v[164:167], v[36:51]
	v_exp_f32_e32 v59, v138
	v_exp_f32_e32 v56, v123
	v_exp_f32_e32 v123, v124
	v_exp_f32_e32 v124, v140
	v_cvt_pk_bf16_f32 v57, v118, v91
	v_cvt_pk_bf16_f32 v87, v121, v56
	v_cvt_pk_bf16_f32 v56, v98, v116
	v_mfma_f32_32x32x16_bf16 v[68:83], v[236:239], v[164:167], v[68:83]
	v_cvt_pk_bf16_f32 v58, v93, v120
	v_cvt_pk_bf16_f32 v59, v59, v122
	v_cvt_pk_bf16_f32 v60, v123, v125
	v_cvt_pk_bf16_f32 v52, v124, v132
	v_mov_b64_e32 v[126:127], s[94:95]
	v_mov_b64_e32 v[124:125], s[92:93]
	v_max3_f32 v96, v36, v37, v68
	v_max_f32_e32 v97, v51, v51
	v_max3_f32 v96, v96, v69, v38
	ds_read_b64_tr_b16 v[120:121], v234 offset:0
	ds_read_b64_tr_b16 v[122:123], v234 offset:1024
	s_nop 0
	v_mfma_f32_32x32x16_bf16 v[100:115], v[124:127], v[84:87], v[100:115]
	v_max3_f32 v96, v96, v70, v71
	ds_read_b64_tr_b16 v[116:117], v235 offset:0
	ds_read_b64_tr_b16 v[118:119], v235 offset:1024
	ds_read_b64_tr_b16 v[92:93], v234 offset:2048
	ds_read_b64_tr_b16 v[94:95], v234 offset:3072
	ds_read_b64_tr_b16 v[88:89], v235 offset:2048
	s_nop 0
	v_max3_f32 v96, v96, v39, v40
	v_mfma_f32_32x32x16_bf16 v[100:115], v[124:127], v[60:63], v[100:115]
	v_max3_f32 v96, v96, v72, v73
	ds_read_b64_tr_b16 v[90:91], v235 offset:3072
	s_nop 0
	v_max3_f32 v96, v96, v41, v42
	s_nop 0
	v_max3_f32 v96, v96, v74, v75
	s_nop 0
	v_max3_f32 v96, v96, v43, v44
	v_mfma_f32_32x32x16_bf16 v[100:115], v[124:127], v[56:59], v[100:115]
	v_max3_f32 v96, v96, v76, v77
	s_nop 0
	v_max3_f32 v96, v96, v45, v46
	s_nop 0
	v_max3_f32 v96, v96, v78, v79
	s_nop 0
	v_max3_f32 v96, v96, v47, v48
	v_mfma_f32_32x32x16_bf16 v[100:115], v[124:127], v[52:55], v[100:115]
	v_max3_f32 v96, v96, v80, v81
	s_nop 0
	v_max3_f32 v96, v96, v49, v50
	s_nop 0
	v_max3_f32 v96, v96, v82, v83
	s_nop 0
	ds_read_b64_tr_b16 v[180:181], v234 offset:4096
	ds_read_b64_tr_b16 v[182:183], v234 offset:5120
	ds_read_b64_tr_b16 v[218:219], v235 offset:4096
	ds_read_b64_tr_b16 v[220:221], v235 offset:5120
	ds_read_b64_tr_b16 v[240:241], v234 offset:6144
	ds_read_b64_tr_b16 v[242:243], v234 offset:7168
	ds_read_b64_tr_b16 v[244:245], v235 offset:6144
	ds_read_b64_tr_b16 v[246:247], v235 offset:7168
	v_max_f32_e32 v96, v96, v96
	v_max_f32_e32 v96, v96, v97
	v_mov_b32_e32 v97, v96
	s_nop 1
	v_permlane32_swap_b32_e32 v96, v97
	v_sub_f32_e32 v96, v96, v66
	s_waitcnt lgkmcnt(0)
	s_nop 0
	v_mfma_f32_32x32x16_bf16 v[2:17], v[120:123], v[84:87], v[2:17]
	v_mfma_f32_32x32x16_bf16 v[18:33], v[116:119], v[84:87], v[18:33]
	v_mfma_f32_32x32x16_bf16 v[2:17], v[92:95], v[60:63], v[2:17]
	v_mfma_f32_32x32x16_bf16 v[18:33], v[88:91], v[60:63], v[18:33]
	s_nop 0
	s_waitcnt lgkmcnt(0)
	s_nop 0
	v_mfma_f32_32x32x16_bf16 v[2:17], v[180:183], v[56:59], v[2:17]
	v_mfma_f32_32x32x16_bf16 v[18:33], v[218:221], v[56:59], v[18:33]
	v_mfma_f32_32x32x16_bf16 v[2:17], v[240:243], v[52:55], v[2:17]
	v_mfma_f32_32x32x16_bf16 v[18:33], v[244:247], v[52:55], v[18:33]
	v_cmp_lt_f32_e32 vcc, s29, v96
	s_cbranch_vccz .LBB0_1600
	v_max_f32_e32 v52, v96, v96
	v_max_f32_e32 v53, 0, v52
	v_exp_f32_e64 v52, -v53
	v_add_f32_e32 v66, v66, v53
	v_mul_f32_e32 v34, v34, v52
	v_pk_mul_f32 v[114:115], v[114:115], v[52:53] op_sel_hi:[1,0]
	v_pk_mul_f32 v[112:113], v[112:113], v[52:53] op_sel_hi:[1,0]
	v_pk_mul_f32 v[110:111], v[110:111], v[52:53] op_sel_hi:[1,0]
	v_pk_mul_f32 v[108:109], v[108:109], v[52:53] op_sel_hi:[1,0]
	v_pk_mul_f32 v[106:107], v[106:107], v[52:53] op_sel_hi:[1,0]
	v_pk_mul_f32 v[104:105], v[104:105], v[52:53] op_sel_hi:[1,0]
	v_pk_mul_f32 v[102:103], v[102:103], v[52:53] op_sel_hi:[1,0]
	v_pk_mul_f32 v[100:101], v[100:101], v[52:53] op_sel_hi:[1,0]
	v_pk_mul_f32 v[32:33], v[52:53], v[32:33] op_sel_hi:[0,1]
	v_pk_mul_f32 v[30:31], v[52:53], v[30:31] op_sel_hi:[0,1]
	v_pk_mul_f32 v[28:29], v[52:53], v[28:29] op_sel_hi:[0,1]
	v_pk_mul_f32 v[26:27], v[52:53], v[26:27] op_sel_hi:[0,1]
	v_pk_mul_f32 v[24:25], v[52:53], v[24:25] op_sel_hi:[0,1]
	v_pk_mul_f32 v[22:23], v[52:53], v[22:23] op_sel_hi:[0,1]
	v_pk_mul_f32 v[20:21], v[52:53], v[20:21] op_sel_hi:[0,1]
	v_pk_mul_f32 v[18:19], v[52:53], v[18:19] op_sel_hi:[0,1]
	v_pk_mul_f32 v[16:17], v[52:53], v[16:17] op_sel_hi:[0,1]
	v_pk_mul_f32 v[14:15], v[52:53], v[14:15] op_sel_hi:[0,1]
	v_pk_mul_f32 v[12:13], v[52:53], v[12:13] op_sel_hi:[0,1]
	v_pk_mul_f32 v[10:11], v[52:53], v[10:11] op_sel_hi:[0,1]
	v_pk_mul_f32 v[8:9], v[52:53], v[8:9] op_sel_hi:[0,1]
	v_pk_mul_f32 v[6:7], v[52:53], v[6:7] op_sel_hi:[0,1]
	v_pk_mul_f32 v[4:5], v[52:53], v[4:5] op_sel_hi:[0,1]
	v_pk_mul_f32 v[2:3], v[52:53], v[2:3] op_sel_hi:[0,1]

.LBB0_1631:
	s_mov_b32 s31, s89
	ds_read_b128 v[52:55], v211
	ds_read_b128 v[56:59], v211 offset:32
	v_exp_f32_e32 v36, v36
	v_exp_f32_e32 v68, v68
	v_exp_f32_e32 v37, v37
	s_waitcnt lgkmcnt(0)
	v_mfma_f32_32x32x16_bf16 v[116:131], v[52:55], v[168:171], 0
	ds_read_b128 v[52:55], v211 offset:6144
	ds_read_b128 v[60:63], v211 offset:6176
	v_exp_f32_e32 v69, v69
	v_exp_f32_e32 v38, v38
	v_exp_f32_e32 v70, v70
	v_exp_f32_e32 v39, v39
	v_exp_f32_e32 v71, v71
	v_exp_f32_e32 v40, v40
	s_waitcnt lgkmcnt(0)
	v_mfma_f32_32x32x16_bf16 v[132:147], v[52:55], v[168:171], 0
	v_exp_f32_e32 v72, v72
	v_exp_f32_e32 v41, v41
	v_exp_f32_e32 v73, v73
	v_exp_f32_e32 v42, v42
	v_exp_f32_e32 v43, v43
	v_exp_f32_e32 v44, v44
	v_exp_f32_e32 v45, v45
	v_mfma_f32_32x32x16_bf16 v[116:131], v[56:59], v[148:151], v[116:131]
	ds_read_b128 v[52:55], v211 offset:64
	ds_read_b128 v[56:59], v211 offset:96
	v_exp_f32_e32 v46, v46
	v_exp_f32_e32 v47, v47
	v_cvt_pk_bf16_f32 v44, v44, v45
	v_cvt_pk_bf16_f32 v45, v46, v47
	v_mfma_f32_32x32x16_bf16 v[132:147], v[60:63], v[148:151], v[132:147]
	v_exp_f32_e32 v60, v78
	v_exp_f32_e32 v61, v79
	v_exp_f32_e32 v62, v48
	v_exp_f32_e32 v63, v80
	v_cvt_pk_bf16_f32 v48, v36, v37
	v_cvt_pk_bf16_f32 v37, v60, v61
	s_waitcnt lgkmcnt(0)
	v_mfma_f32_32x32x16_bf16 v[116:131], v[52:55], v[152:155], v[116:131]
	ds_read_b128 v[52:55], v211 offset:6208
	ds_read_b128 v[84:87], v211 offset:6240
	ds_read_b128 v[88:91], v226
	ds_read_b128 v[92:95], v226 offset:6144
	s_waitcnt lgkmcnt(0)
	v_mfma_f32_32x32x16_bf16 v[132:147], v[52:55], v[152:155], v[132:147]
	v_exp_f32_e32 v52, v81
	v_exp_f32_e32 v53, v50
	v_exp_f32_e32 v54, v82
	v_exp_f32_e32 v55, v51
	v_cvt_pk_bf16_f32 v50, v40, v41
	v_cvt_pk_bf16_f32 v51, v42, v43
	v_cvt_pk_bf16_f32 v40, v68, v69
	v_mfma_f32_32x32x16_bf16 v[116:131], v[56:59], v[156:159], v[116:131]
	ds_read_b128 v[56:59], v227
	ds_read_b128 v[236:239], v227 offset:6144
	v_cvt_pk_bf16_f32 v41, v70, v71
	v_cvt_pk_bf16_f32 v42, v72, v73
	v_cvt_pk_bf16_f32 v47, v53, v55
	v_mfma_f32_32x32x16_bf16 v[132:147], v[84:87], v[156:159], v[132:147]
	v_mfma_f32_32x32x16_bf16 v[116:131], v[88:91], v[160:163], v[116:131]
	v_mfma_f32_32x32x16_bf16 v[132:147], v[92:95], v[160:163], v[132:147]
	s_waitcnt lgkmcnt(0)
	v_mfma_f32_32x32x16_bf16 v[116:131], v[56:59], v[164:167], v[116:131]
	v_exp_f32_e32 v56, v74
	v_exp_f32_e32 v57, v75
	v_exp_f32_e32 v58, v76
	v_exp_f32_e32 v59, v77
	v_exp_f32_e32 v74, v49
	v_exp_f32_e32 v75, v83
	v_cvt_pk_bf16_f32 v49, v38, v39
	v_mfma_f32_32x32x16_bf16 v[132:147], v[236:239], v[164:167], v[132:147]
	v_cvt_pk_bf16_f32 v43, v56, v57
	v_cvt_pk_bf16_f32 v46, v62, v74
	v_cvt_pk_bf16_f32 v36, v58, v59
	v_cvt_pk_bf16_f32 v38, v63, v52
	v_cvt_pk_bf16_f32 v39, v54, v75
	v_mov_b64_e32 v[74:75], s[92:93]
	v_mov_b64_e32 v[76:77], s[94:95]
	v_max3_f32 v72, v116, v117, v132
	v_max_f32_e32 v73, v131, v131
	v_max3_f32 v72, v72, v133, v118
	ds_read_b64_tr_b16 v[68:69], v205 offset:0
	ds_read_b64_tr_b16 v[70:71], v205 offset:1024
	s_nop 0
	v_mfma_f32_32x32x16_bf16 v[100:115], v[74:77], v[48:51], v[100:115]
	v_max3_f32 v72, v72, v134, v135
	ds_read_b64_tr_b16 v[60:61], v67 offset:0
	ds_read_b64_tr_b16 v[62:63], v67 offset:1024
	ds_read_b64_tr_b16 v[56:57], v205 offset:2048
	ds_read_b64_tr_b16 v[58:59], v205 offset:3072
	ds_read_b64_tr_b16 v[52:53], v67 offset:2048
	s_nop 0
	v_max3_f32 v72, v72, v119, v120
	v_mfma_f32_32x32x16_bf16 v[100:115], v[74:77], v[44:47], v[100:115]
	v_max3_f32 v72, v72, v136, v137
	ds_read_b64_tr_b16 v[54:55], v67 offset:3072
	s_nop 0
	v_max3_f32 v72, v72, v121, v122
	s_nop 0
	v_max3_f32 v72, v72, v138, v139
	s_nop 0
	v_max3_f32 v72, v72, v123, v124
	v_mfma_f32_32x32x16_bf16 v[100:115], v[74:77], v[40:43], v[100:115]
	v_max3_f32 v72, v72, v140, v141
	s_nop 0
	v_max3_f32 v72, v72, v125, v126
	s_nop 0
	v_max3_f32 v72, v72, v142, v143
	s_nop 0
	v_max3_f32 v72, v72, v127, v128
	v_mfma_f32_32x32x16_bf16 v[100:115], v[74:77], v[36:39], v[100:115]
	v_max3_f32 v72, v72, v144, v145
	s_nop 0
	v_max3_f32 v72, v72, v129, v130
	s_nop 0
	v_max3_f32 v72, v72, v146, v147
	s_nop 0
	ds_read_b64_tr_b16 v[180:181], v205 offset:4096
	ds_read_b64_tr_b16 v[182:183], v205 offset:5120
	ds_read_b64_tr_b16 v[218:219], v67 offset:4096
	ds_read_b64_tr_b16 v[220:221], v67 offset:5120
	ds_read_b64_tr_b16 v[240:241], v205 offset:6144
	ds_read_b64_tr_b16 v[242:243], v205 offset:7168
	ds_read_b64_tr_b16 v[244:245], v67 offset:6144
	ds_read_b64_tr_b16 v[246:247], v67 offset:7168
	v_max_f32_e32 v72, v72, v72
	v_max_f32_e32 v72, v72, v73
	v_mov_b32_e32 v73, v72
	s_nop 1
	v_permlane32_swap_b32_e32 v72, v73
	v_sub_f32_e32 v72, v72, v66
	s_waitcnt lgkmcnt(0)
	s_nop 0
	v_mfma_f32_32x32x16_bf16 v[2:17], v[68:71], v[48:51], v[2:17]
	v_mfma_f32_32x32x16_bf16 v[18:33], v[60:63], v[48:51], v[18:33]
	v_mfma_f32_32x32x16_bf16 v[2:17], v[56:59], v[44:47], v[2:17]
	v_mfma_f32_32x32x16_bf16 v[18:33], v[52:55], v[44:47], v[18:33]
	s_nop 0
	s_waitcnt lgkmcnt(0)
	s_nop 0
	v_mfma_f32_32x32x16_bf16 v[2:17], v[180:183], v[40:43], v[2:17]
	v_mfma_f32_32x32x16_bf16 v[18:33], v[218:221], v[40:43], v[18:33]
	v_mfma_f32_32x32x16_bf16 v[2:17], v[240:243], v[36:39], v[2:17]
	v_mfma_f32_32x32x16_bf16 v[18:33], v[244:247], v[36:39], v[18:33]
	v_cmp_lt_f32_e32 vcc, s29, v72
	s_cbranch_vccz .LBB0_1633
	v_max_f32_e32 v36, v72, v72
	v_max_f32_e32 v37, 0, v36
	v_exp_f32_e64 v36, -v37
	v_add_f32_e32 v66, v66, v37
	v_mul_f32_e32 v34, v34, v36
	v_pk_mul_f32 v[114:115], v[114:115], v[36:37] op_sel_hi:[1,0]
	v_pk_mul_f32 v[112:113], v[112:113], v[36:37] op_sel_hi:[1,0]
	v_pk_mul_f32 v[110:111], v[110:111], v[36:37] op_sel_hi:[1,0]
	v_pk_mul_f32 v[108:109], v[108:109], v[36:37] op_sel_hi:[1,0]
	v_pk_mul_f32 v[106:107], v[106:107], v[36:37] op_sel_hi:[1,0]
	v_pk_mul_f32 v[104:105], v[104:105], v[36:37] op_sel_hi:[1,0]
	v_pk_mul_f32 v[102:103], v[102:103], v[36:37] op_sel_hi:[1,0]
	v_pk_mul_f32 v[100:101], v[100:101], v[36:37] op_sel_hi:[1,0]
	v_pk_mul_f32 v[32:33], v[36:37], v[32:33] op_sel_hi:[0,1]
	v_pk_mul_f32 v[30:31], v[36:37], v[30:31] op_sel_hi:[0,1]
	v_pk_mul_f32 v[28:29], v[36:37], v[28:29] op_sel_hi:[0,1]
	v_pk_mul_f32 v[26:27], v[36:37], v[26:27] op_sel_hi:[0,1]
	v_pk_mul_f32 v[24:25], v[36:37], v[24:25] op_sel_hi:[0,1]
	v_pk_mul_f32 v[22:23], v[36:37], v[22:23] op_sel_hi:[0,1]
	v_pk_mul_f32 v[20:21], v[36:37], v[20:21] op_sel_hi:[0,1]
	v_pk_mul_f32 v[18:19], v[36:37], v[18:19] op_sel_hi:[0,1]
	v_pk_mul_f32 v[16:17], v[36:37], v[16:17] op_sel_hi:[0,1]
	v_pk_mul_f32 v[14:15], v[36:37], v[14:15] op_sel_hi:[0,1]
	v_pk_mul_f32 v[12:13], v[36:37], v[12:13] op_sel_hi:[0,1]
	v_pk_mul_f32 v[10:11], v[36:37], v[10:11] op_sel_hi:[0,1]
	v_pk_mul_f32 v[8:9], v[36:37], v[8:9] op_sel_hi:[0,1]
	v_pk_mul_f32 v[6:7], v[36:37], v[6:7] op_sel_hi:[0,1]
	v_pk_mul_f32 v[4:5], v[36:37], v[4:5] op_sel_hi:[0,1]
	v_pk_mul_f32 v[2:3], v[36:37], v[2:3] op_sel_hi:[0,1]

.LBB0_2006:
	v_mov_b64_e32 v[88:89], s[92:93]
	v_mov_b64_e32 v[90:91], s[94:95]
	v_max3_f32 v86, v100, v101, v116
	v_max_f32_e32 v87, v115, v115
	v_max3_f32 v86, v86, v117, v102
	s_nop 0
	v_mfma_f32_32x32x16_bf16 v[34:49], v[88:91], v[58:61], v[34:49]
	v_max3_f32 v86, v86, v118, v119
	s_nop 0
	v_max3_f32 v86, v86, v103, v104
	s_nop 0
	v_max3_f32 v86, v86, v120, v121
	s_nop 0
	v_max3_f32 v86, v86, v105, v106
	v_mfma_f32_32x32x16_bf16 v[34:49], v[88:91], v[62:65], v[34:49]
	v_max3_f32 v86, v86, v122, v123
	s_nop 0
	v_max3_f32 v86, v86, v107, v108
	s_nop 0
	v_max3_f32 v86, v86, v124, v125
	s_nop 0
	v_max3_f32 v86, v86, v109, v110
	v_mfma_f32_32x32x16_bf16 v[34:49], v[88:91], v[54:57], v[34:49]
	v_max3_f32 v86, v86, v126, v127
	s_nop 0
	v_max3_f32 v86, v86, v111, v112
	s_nop 0
	v_max3_f32 v86, v86, v128, v129
	s_nop 0
	v_max3_f32 v86, v86, v113, v114
	v_mfma_f32_32x32x16_bf16 v[34:49], v[88:91], v[50:53], v[34:49]
	v_max3_f32 v86, v86, v130, v131
	s_nop 0
	ds_read_b64_tr_b16 v[226:227], v200 offset:4096
	ds_read_b64_tr_b16 v[228:229], v200 offset:5120
	ds_read_b64_tr_b16 v[230:231], v201 offset:4096
	ds_read_b64_tr_b16 v[232:233], v201 offset:5120
	ds_read_b64_tr_b16 v[234:235], v200 offset:6144
	ds_read_b64_tr_b16 v[236:237], v200 offset:7168
	ds_read_b64_tr_b16 v[238:239], v201 offset:6144
	ds_read_b64_tr_b16 v[240:241], v201 offset:7168
	v_max_f32_e32 v86, v86, v86
	v_max_f32_e32 v86, v86, v87
	v_mov_b32_e32 v87, v86
	s_nop 1
	v_permlane32_swap_b32_e32 v86, v87
	v_sub_f32_e32 v86, v86, v184
	s_waitcnt lgkmcnt(0)
	s_nop 0
	v_mfma_f32_32x32x16_bf16 v[18:33], v[78:81], v[58:61], v[18:33]
	v_mfma_f32_32x32x16_bf16 v[2:17], v[74:77], v[58:61], v[2:17]
	v_mfma_f32_32x32x16_bf16 v[18:33], v[70:73], v[62:65], v[18:33]
	v_mfma_f32_32x32x16_bf16 v[2:17], v[66:69], v[62:65], v[2:17]
	s_nop 0
	s_waitcnt lgkmcnt(0)
	s_nop 0
	v_mfma_f32_32x32x16_bf16 v[18:33], v[226:229], v[54:57], v[18:33]
	v_mfma_f32_32x32x16_bf16 v[2:17], v[230:233], v[54:57], v[2:17]
	v_mfma_f32_32x32x16_bf16 v[18:33], v[234:237], v[50:53], v[18:33]
	v_mfma_f32_32x32x16_bf16 v[2:17], v[238:241], v[50:53], v[2:17]
	v_cmp_lt_f32_e32 vcc, s29, v86
	s_cbranch_vccz .LBB0_2008
	v_max_f32_e32 v50, v86, v86
	v_max_f32_e32 v51, 0, v50
	v_exp_f32_e64 v50, -v51
	v_add_f32_e32 v184, v184, v51
	v_mul_f32_e32 v175, v175, v50
	v_pk_mul_f32 v[48:49], v[48:49], v[50:51] op_sel_hi:[1,0]
	v_pk_mul_f32 v[46:47], v[46:47], v[50:51] op_sel_hi:[1,0]
	v_pk_mul_f32 v[44:45], v[44:45], v[50:51] op_sel_hi:[1,0]
	v_pk_mul_f32 v[42:43], v[42:43], v[50:51] op_sel_hi:[1,0]
	v_pk_mul_f32 v[40:41], v[40:41], v[50:51] op_sel_hi:[1,0]
	v_pk_mul_f32 v[38:39], v[38:39], v[50:51] op_sel_hi:[1,0]
	v_pk_mul_f32 v[36:37], v[36:37], v[50:51] op_sel_hi:[1,0]
	v_pk_mul_f32 v[34:35], v[34:35], v[50:51] op_sel_hi:[1,0]
	v_pk_mul_f32 v[16:17], v[50:51], v[16:17] op_sel_hi:[0,1]
	v_pk_mul_f32 v[14:15], v[50:51], v[14:15] op_sel_hi:[0,1]
	v_pk_mul_f32 v[12:13], v[50:51], v[12:13] op_sel_hi:[0,1]
	v_pk_mul_f32 v[10:11], v[50:51], v[10:11] op_sel_hi:[0,1]
	v_pk_mul_f32 v[8:9], v[50:51], v[8:9] op_sel_hi:[0,1]
	v_pk_mul_f32 v[6:7], v[50:51], v[6:7] op_sel_hi:[0,1]
	v_pk_mul_f32 v[4:5], v[50:51], v[4:5] op_sel_hi:[0,1]
	v_pk_mul_f32 v[2:3], v[50:51], v[2:3] op_sel_hi:[0,1]
	v_pk_mul_f32 v[32:33], v[50:51], v[32:33] op_sel_hi:[0,1]
	v_pk_mul_f32 v[30:31], v[50:51], v[30:31] op_sel_hi:[0,1]
	v_pk_mul_f32 v[28:29], v[50:51], v[28:29] op_sel_hi:[0,1]
	v_pk_mul_f32 v[26:27], v[50:51], v[26:27] op_sel_hi:[0,1]
	v_pk_mul_f32 v[24:25], v[50:51], v[24:25] op_sel_hi:[0,1]
	v_pk_mul_f32 v[22:23], v[50:51], v[22:23] op_sel_hi:[0,1]
	v_pk_mul_f32 v[20:21], v[50:51], v[20:21] op_sel_hi:[0,1]
	v_pk_mul_f32 v[18:19], v[50:51], v[18:19] op_sel_hi:[0,1]

.LBB0_2044:
	v_mov_b64_e32 v[124:125], s[94:95]
	v_mov_b64_e32 v[122:123], s[92:93]
	v_max3_f32 v98, v50, v51, v66
	v_max_f32_e32 v120, v65, v65
	v_max3_f32 v98, v98, v67, v52
	s_nop 0
	v_mfma_f32_32x32x16_bf16 v[34:49], v[122:125], v[94:97], v[34:49]
	v_max3_f32 v98, v98, v68, v69
	s_nop 0
	v_max3_f32 v98, v98, v53, v54
	s_nop 0
	v_max3_f32 v98, v98, v70, v71
	s_nop 0
	v_max3_f32 v98, v98, v55, v56
	v_mfma_f32_32x32x16_bf16 v[34:49], v[122:125], v[100:103], v[34:49]
	v_max3_f32 v98, v98, v72, v73
	s_nop 0
	v_max3_f32 v98, v98, v57, v58
	s_nop 0
	v_max3_f32 v98, v98, v74, v75
	s_nop 0
	v_max3_f32 v98, v98, v59, v60
	v_mfma_f32_32x32x16_bf16 v[34:49], v[122:125], v[90:93], v[34:49]
	v_max3_f32 v98, v98, v76, v77
	s_nop 0
	v_max3_f32 v98, v98, v61, v62
	s_nop 0
	v_max3_f32 v98, v98, v78, v79
	s_nop 0
	v_max3_f32 v98, v98, v63, v64
	v_mfma_f32_32x32x16_bf16 v[34:49], v[122:125], v[86:89], v[34:49]
	v_max3_f32 v98, v98, v80, v81
	s_nop 0
	ds_read_b64_tr_b16 v[226:227], v202 offset:4096
	ds_read_b64_tr_b16 v[228:229], v202 offset:5120
	ds_read_b64_tr_b16 v[230:231], v203 offset:4096
	ds_read_b64_tr_b16 v[232:233], v203 offset:5120
	ds_read_b64_tr_b16 v[234:235], v202 offset:6144
	ds_read_b64_tr_b16 v[236:237], v202 offset:7168
	ds_read_b64_tr_b16 v[238:239], v203 offset:6144
	ds_read_b64_tr_b16 v[240:241], v203 offset:7168
	v_max_f32_e32 v98, v98, v98
	v_max_f32_e32 v98, v98, v120
	v_mov_b32_e32 v120, v98
	s_nop 1
	v_permlane32_swap_b32_e32 v98, v120
	v_sub_f32_e32 v120, v98, v184
	s_waitcnt lgkmcnt(0)
	s_nop 0
	v_mfma_f32_32x32x16_bf16 v[18:33], v[116:119], v[94:97], v[18:33]
	v_mfma_f32_32x32x16_bf16 v[2:17], v[112:115], v[94:97], v[2:17]
	v_mfma_f32_32x32x16_bf16 v[18:33], v[108:111], v[100:103], v[18:33]
	v_mfma_f32_32x32x16_bf16 v[2:17], v[104:107], v[100:103], v[2:17]
	s_nop 0
	s_waitcnt lgkmcnt(0)
	s_nop 0
	v_mfma_f32_32x32x16_bf16 v[18:33], v[226:229], v[90:93], v[18:33]
	v_mfma_f32_32x32x16_bf16 v[2:17], v[230:233], v[90:93], v[2:17]
	v_mfma_f32_32x32x16_bf16 v[18:33], v[234:237], v[86:89], v[18:33]
	v_mfma_f32_32x32x16_bf16 v[2:17], v[238:241], v[86:89], v[2:17]
	v_cmp_lt_f32_e32 vcc, s29, v120
	s_cbranch_vccz .LBB0_2046
	v_max_f32_e32 v86, v120, v120
	v_max_f32_e32 v87, 0, v86
	v_exp_f32_e64 v86, -v87
	v_add_f32_e32 v184, v184, v87
	v_mul_f32_e32 v175, v175, v86
	v_pk_mul_f32 v[48:49], v[48:49], v[86:87] op_sel_hi:[1,0]
	v_pk_mul_f32 v[46:47], v[46:47], v[86:87] op_sel_hi:[1,0]
	v_pk_mul_f32 v[44:45], v[44:45], v[86:87] op_sel_hi:[1,0]
	v_pk_mul_f32 v[42:43], v[42:43], v[86:87] op_sel_hi:[1,0]
	v_pk_mul_f32 v[40:41], v[40:41], v[86:87] op_sel_hi:[1,0]
	v_pk_mul_f32 v[38:39], v[38:39], v[86:87] op_sel_hi:[1,0]
	v_pk_mul_f32 v[36:37], v[36:37], v[86:87] op_sel_hi:[1,0]
	v_pk_mul_f32 v[34:35], v[34:35], v[86:87] op_sel_hi:[1,0]
	v_pk_mul_f32 v[16:17], v[86:87], v[16:17] op_sel_hi:[0,1]
	v_pk_mul_f32 v[14:15], v[86:87], v[14:15] op_sel_hi:[0,1]
	v_pk_mul_f32 v[12:13], v[86:87], v[12:13] op_sel_hi:[0,1]
	v_pk_mul_f32 v[10:11], v[86:87], v[10:11] op_sel_hi:[0,1]
	v_pk_mul_f32 v[8:9], v[86:87], v[8:9] op_sel_hi:[0,1]
	v_pk_mul_f32 v[6:7], v[86:87], v[6:7] op_sel_hi:[0,1]
	v_pk_mul_f32 v[4:5], v[86:87], v[4:5] op_sel_hi:[0,1]
	v_pk_mul_f32 v[2:3], v[86:87], v[2:3] op_sel_hi:[0,1]
	v_pk_mul_f32 v[32:33], v[86:87], v[32:33] op_sel_hi:[0,1]
	v_pk_mul_f32 v[30:31], v[86:87], v[30:31] op_sel_hi:[0,1]
	v_pk_mul_f32 v[28:29], v[86:87], v[28:29] op_sel_hi:[0,1]
	v_pk_mul_f32 v[26:27], v[86:87], v[26:27] op_sel_hi:[0,1]
	v_pk_mul_f32 v[24:25], v[86:87], v[24:25] op_sel_hi:[0,1]
	v_pk_mul_f32 v[22:23], v[86:87], v[22:23] op_sel_hi:[0,1]
	v_pk_mul_f32 v[20:21], v[86:87], v[20:21] op_sel_hi:[0,1]
	v_pk_mul_f32 v[18:19], v[86:87], v[18:19] op_sel_hi:[0,1]
